# baseline (speedup 1.0000x reference)
_Z11k_csr_gemm1PKjPK15HIP_vector_typeIiLj2EEPS2_PiS6_PfS6_PKfPKDv8_DF16_PDF16_:
	s_mov_b64 s[4:5], -1
	s_cmpk_gt_u32 s2, 0x186
	v_lshrrev_b32_e32 v1, 6, v0
	v_and_b32_e32 v88, 63, v0
	s_cbranch_scc0 .LBB1_42
	s_load_dwordx4 s[4:7], s[0:1], 0x38
	v_lshlrev_b32_e32 v82, 4, v0
	s_lshl_b32 s3, s2, 6
	v_lshrrev_b32_e32 v89, 6, v0
	s_addk_i32 s3, 0x9e40
	v_lshlrev_b32_e32 v66, 4, v88
	v_mov_b32_e32 v67, 0
	v_or_b32_e32 v86, s3, v89
	s_movk_i32 s8, 0x400
	s_mov_b32 s9, 0xc34f
	s_waitcnt lgkmcnt(0)
	v_lshl_add_u64 v[84:85], s[4:5], 0, v[66:67]
	v_min_u32_e32 v92, s9, v86
	v_mad_u64_u32 v[92:93], s[12:13], v92, s8, v[84:85]
	global_load_dwordx4 v[66:69], v[92:93], off nt
	v_add_u32_e32 v94, 4, v86
	v_min_u32_e32 v94, s9, v94
	v_mad_u64_u32 v[94:95], s[12:13], v94, s8, v[84:85]
	global_load_dwordx4 v[70:73], v[94:95], off nt
	v_add_u32_e32 v92, 8, v86
	v_min_u32_e32 v92, s9, v92
	v_mad_u64_u32 v[92:93], s[12:13], v92, s8, v[84:85]
	global_load_dwordx4 v[74:77], v[92:93], off nt
	v_add_u32_e32 v94, 12, v86
	v_min_u32_e32 v94, s9, v94
	v_mad_u64_u32 v[94:95], s[12:13], v94, s8, v[84:85]
	global_load_dwordx4 v[78:81], v[94:95], off nt
	v_add_u32_e32 v92, 16, v86
	v_min_u32_e32 v92, s9, v92
	v_mad_u64_u32 v[92:93], s[12:13], v92, s8, v[84:85]
	global_load_dwordx4 a[0:3], v[92:93], off nt
	v_add_u32_e32 v94, 20, v86
	v_min_u32_e32 v94, s9, v94
	v_mad_u64_u32 v[94:95], s[12:13], v94, s8, v[84:85]
	global_load_dwordx4 a[4:7], v[94:95], off nt
	v_add_u32_e32 v92, 24, v86
	v_min_u32_e32 v92, s9, v92
	v_mad_u64_u32 v[92:93], s[12:13], v92, s8, v[84:85]
	global_load_dwordx4 a[8:11], v[92:93], off nt
	v_add_u32_e32 v94, 28, v86
	v_min_u32_e32 v94, s9, v94
	v_mad_u64_u32 v[94:95], s[12:13], v94, s8, v[84:85]
	global_load_dwordx4 a[12:15], v[94:95], off nt
	v_add_u32_e32 v92, 32, v86
	v_min_u32_e32 v92, s9, v92
	v_mad_u64_u32 v[92:93], s[12:13], v92, s8, v[84:85]
	global_load_dwordx4 a[16:19], v[92:93], off nt
	v_add_u32_e32 v94, 36, v86
	v_min_u32_e32 v94, s9, v94
	v_mad_u64_u32 v[94:95], s[12:13], v94, s8, v[84:85]
	global_load_dwordx4 a[20:23], v[94:95], off nt
	v_add_u32_e32 v92, 40, v86
	v_min_u32_e32 v92, s9, v92
	v_mad_u64_u32 v[92:93], s[12:13], v92, s8, v[84:85]
	global_load_dwordx4 a[24:27], v[92:93], off nt
	v_add_u32_e32 v94, 44, v86
	v_min_u32_e32 v94, s9, v94
	v_mad_u64_u32 v[94:95], s[12:13], v94, s8, v[84:85]
	global_load_dwordx4 a[28:31], v[94:95], off nt
	v_mov_b32_e32 v83, 0
	v_lshl_add_u64 v[6:7], s[6:7], 0, v[82:83]
	v_add_co_u32_e32 v2, vcc, 0x1000, v6
	s_nop 0
	v_addc_co_u32_e32 v3, vcc, 0, v7, vcc
	v_add_co_u32_e32 v4, vcc, 0x2000, v6
	s_nop 0
	v_addc_co_u32_e32 v5, vcc, 0, v7, vcc
	global_load_dwordx4 v[58:61], v[2:3], off
	global_load_dwordx4 v[34:37], v[4:5], off
	v_add_co_u32_e32 v2, vcc, 0x3000, v6
	s_nop 0
	v_addc_co_u32_e32 v3, vcc, 0, v7, vcc
	v_add_co_u32_e32 v4, vcc, 0x4000, v6
	s_nop 0
	v_addc_co_u32_e32 v5, vcc, 0, v7, vcc
	global_load_dwordx4 v[54:57], v[2:3], off
	global_load_dwordx4 v[30:33], v[4:5], off
	v_add_co_u32_e32 v2, vcc, 0x5000, v6
	s_nop 0
	v_addc_co_u32_e32 v3, vcc, 0, v7, vcc
	v_add_co_u32_e32 v4, vcc, 0x6000, v6
	s_nop 1
	v_addc_co_u32_e32 v5, vcc, 0, v7, vcc
	global_load_dwordx4 v[50:53], v[2:3], off
	global_load_dwordx4 v[26:29], v[4:5], off
	v_add_co_u32_e32 v2, vcc, 0x7000, v6
	s_nop 1
	v_addc_co_u32_e32 v3, vcc, 0, v7, vcc
	v_add_co_u32_e32 v4, vcc, 0x8000, v6
	s_nop 1
	v_addc_co_u32_e32 v5, vcc, 0, v7, vcc
	global_load_dwordx4 v[46:49], v[2:3], off
	global_load_dwordx4 v[22:25], v[4:5], off
	v_add_co_u32_e32 v2, vcc, 0x9000, v6
	s_nop 1
	v_addc_co_u32_e32 v3, vcc, 0, v7, vcc
	v_add_co_u32_e32 v4, vcc, 0xa000, v6
	s_nop 1
	v_addc_co_u32_e32 v5, vcc, 0, v7, vcc
	global_load_dwordx4 v[42:45], v[2:3], off
	global_load_dwordx4 v[18:21], v[4:5], off
	v_add_co_u32_e32 v2, vcc, 0xb000, v6
	s_nop 1
	v_addc_co_u32_e32 v3, vcc, 0, v7, vcc
	v_add_co_u32_e32 v4, vcc, 0xc000, v6
	s_nop 1
	v_addc_co_u32_e32 v5, vcc, 0, v7, vcc
	v_add_co_u32_e32 v8, vcc, 0xd000, v6
	global_load_dwordx4 v[38:41], v[2:3], off
	global_load_dwordx4 v[14:17], v[4:5], off
	v_addc_co_u32_e32 v9, vcc, 0, v7, vcc
	v_add_co_u32_e32 v62, vcc, 0xe000, v6
	s_nop 1
	v_addc_co_u32_e32 v63, vcc, 0, v7, vcc
	v_add_co_u32_e32 v92, vcc, 0xf000, v6
	global_load_dwordx4 v[10:13], v[8:9], off
	global_load_dwordx4 v[2:5], v[62:63], off
	v_addc_co_u32_e32 v93, vcc, 0, v7, vcc
	global_load_dwordx4 v[62:65], v82, s[6:7]
	global_load_dwordx4 v[6:9], v[92:93], off
	s_load_dwordx2 s[4:5], s[0:1], 0x48
	s_movk_i32 s10, 0x210
	v_lshlrev_b32_e32 v90, 3, v88
	v_mad_u32_u24 v83, v89, s10, v90
	s_waitcnt vmcnt(27)
	v_cvt_pk_f16_f32 v66, v66, v67
	v_cvt_pk_f16_f32 v67, v68, v69
	ds_write_b64 v83, v[66:67]
	s_waitcnt vmcnt(26)
	v_cvt_pk_f16_f32 v70, v70, v71
	v_cvt_pk_f16_f32 v71, v72, v73
	ds_write_b64 v83, v[70:71] offset:2112
	s_waitcnt vmcnt(25)
	v_cvt_pk_f16_f32 v74, v74, v75
	v_cvt_pk_f16_f32 v75, v76, v77
	ds_write_b64 v83, v[74:75] offset:4224
	s_waitcnt vmcnt(24)
	v_cvt_pk_f16_f32 v78, v78, v79
	v_cvt_pk_f16_f32 v79, v80, v81
	ds_write_b64 v83, v[78:79] offset:6336
	v_add_u32_e32 v92, 48, v86
	v_min_u32_e32 v92, s9, v92
	v_mad_u64_u32 v[92:93], s[12:13], v92, s8, v[84:85]
	global_load_dwordx4 v[66:69], v[92:93], off nt
	v_add_u32_e32 v94, 52, v86
	v_min_u32_e32 v94, s9, v94
	v_mad_u64_u32 v[94:95], s[12:13], v94, s8, v[84:85]
	global_load_dwordx4 v[70:73], v[94:95], off nt
	v_add_u32_e32 v92, 56, v86
	v_min_u32_e32 v92, s9, v92
	v_mad_u64_u32 v[92:93], s[12:13], v92, s8, v[84:85]
	global_load_dwordx4 v[74:77], v[92:93], off nt
	v_add_u32_e32 v94, 60, v86
	v_min_u32_e32 v94, s9, v94
	v_mad_u64_u32 v[94:95], s[12:13], v94, s8, v[84:85]
	global_load_dwordx4 v[78:81], v[94:95], off nt
	s_waitcnt vmcnt(27)
	v_accvgpr_read_b32 v92, a0
	v_accvgpr_read_b32 v93, a1
	v_accvgpr_read_b32 v94, a2
	v_accvgpr_read_b32 v95, a3
	v_cvt_pk_f16_f32 v92, v92, v93
	v_cvt_pk_f16_f32 v93, v94, v95
	ds_write_b64 v83, v[92:93] offset:8448
	s_waitcnt vmcnt(26)
	v_accvgpr_read_b32 v92, a4
	v_accvgpr_read_b32 v93, a5
	v_accvgpr_read_b32 v94, a6
	v_accvgpr_read_b32 v95, a7
	v_cvt_pk_f16_f32 v92, v92, v93
	v_cvt_pk_f16_f32 v93, v94, v95
	ds_write_b64 v83, v[92:93] offset:10560
	s_waitcnt vmcnt(25)
	v_accvgpr_read_b32 v92, a8
	v_accvgpr_read_b32 v93, a9
	v_accvgpr_read_b32 v94, a10
	v_accvgpr_read_b32 v95, a11
	v_cvt_pk_f16_f32 v92, v92, v93
	v_cvt_pk_f16_f32 v93, v94, v95
	ds_write_b64 v83, v[92:93] offset:12672
	s_waitcnt vmcnt(24)
	v_accvgpr_read_b32 v92, a12
	v_accvgpr_read_b32 v93, a13
	v_accvgpr_read_b32 v94, a14
	v_accvgpr_read_b32 v95, a15
	v_cvt_pk_f16_f32 v92, v92, v93
	v_cvt_pk_f16_f32 v93, v94, v95
	ds_write_b64 v83, v[92:93] offset:14784
	s_waitcnt vmcnt(23)
	v_accvgpr_read_b32 v92, a16
	v_accvgpr_read_b32 v93, a17
	v_accvgpr_read_b32 v94, a18
	v_accvgpr_read_b32 v95, a19
	v_cvt_pk_f16_f32 v92, v92, v93
	v_cvt_pk_f16_f32 v93, v94, v95
	ds_write_b64 v83, v[92:93] offset:16896
	s_waitcnt vmcnt(22)
	v_accvgpr_read_b32 v92, a20
	v_accvgpr_read_b32 v93, a21
	v_accvgpr_read_b32 v94, a22
	v_accvgpr_read_b32 v95, a23
	v_cvt_pk_f16_f32 v92, v92, v93
	v_cvt_pk_f16_f32 v93, v94, v95
	ds_write_b64 v83, v[92:93] offset:19008
	s_waitcnt vmcnt(21)
	v_accvgpr_read_b32 v92, a24
	v_accvgpr_read_b32 v93, a25
	v_accvgpr_read_b32 v94, a26
	v_accvgpr_read_b32 v95, a27
	v_cvt_pk_f16_f32 v92, v92, v93
	v_cvt_pk_f16_f32 v93, v94, v95
	ds_write_b64 v83, v[92:93] offset:21120
	s_waitcnt vmcnt(20)
	v_accvgpr_read_b32 v92, a28
	v_accvgpr_read_b32 v93, a29
	v_accvgpr_read_b32 v94, a30
	v_accvgpr_read_b32 v95, a31
	v_cvt_pk_f16_f32 v92, v92, v93
	v_cvt_pk_f16_f32 v93, v94, v95
	ds_write_b64 v83, v[92:93] offset:23232
	s_waitcnt vmcnt(3)
	v_cvt_pk_f16_f32 v66, v66, v67
	v_cvt_pk_f16_f32 v67, v68, v69
	ds_write_b64 v83, v[66:67] offset:25344
	s_waitcnt vmcnt(2)
	v_cvt_pk_f16_f32 v70, v70, v71
	v_cvt_pk_f16_f32 v71, v72, v73
	ds_write_b64 v83, v[70:71] offset:27456
	s_waitcnt vmcnt(1)
	v_cvt_pk_f16_f32 v74, v74, v75
	v_cvt_pk_f16_f32 v75, v76, v77
	ds_write_b64 v83, v[74:75] offset:29568
	s_waitcnt vmcnt(0)
	v_cvt_pk_f16_f32 v78, v78, v79
	v_cvt_pk_f16_f32 v79, v80, v81
	ds_write_b64 v83, v[78:79] offset:31680
	v_and_b32_e32 v78, 31, v0
	v_lshrrev_b32_e32 v66, 2, v0
	v_and_b32_e32 v79, 8, v66
	v_mul_u32_u24_e32 v66, 0x210, v78
	v_lshl_add_u32 v80, v79, 1, v66
	s_waitcnt lgkmcnt(0)
	s_barrier
	ds_read_b128 v[66:69], v80
	ds_read_b128 v[70:73], v80 offset:32
	s_waitcnt lgkmcnt(1)
	v_mfma_f32_32x32x16_f16 a[16:31], v[62:65], v[66:69], 0
	ds_read_b128 v[66:69], v80 offset:16896
	ds_read_b128 v[74:77], v80 offset:16928
	s_movk_i32 s6, 0xc0
	s_mov_b32 s7, 0xc350
	s_waitcnt lgkmcnt(1)
	v_mfma_f32_32x32x16_f16 a[0:15], v[62:65], v[66:69], 0
	v_mfma_f32_32x32x16_f16 a[16:31], v[58:61], v[70:73], a[16:31]
	s_waitcnt lgkmcnt(0)
	v_mfma_f32_32x32x16_f16 a[0:15], v[58:61], v[74:77], a[0:15]
	ds_read_b128 v[58:61], v80 offset:64
	ds_read_b128 v[62:65], v80 offset:96
	s_waitcnt lgkmcnt(1)
	v_mfma_f32_32x32x16_f16 a[16:31], v[34:37], v[58:61], a[16:31]
	ds_read_b128 v[58:61], v80 offset:16960
	ds_read_b128 v[66:69], v80 offset:16992
	s_waitcnt lgkmcnt(1)
	v_mfma_f32_32x32x16_f16 a[0:15], v[34:37], v[58:61], a[0:15]
	v_mfma_f32_32x32x16_f16 a[16:31], v[54:57], v[62:65], a[16:31]
	s_waitcnt lgkmcnt(0)
	v_mfma_f32_32x32x16_f16 a[0:15], v[54:57], v[66:69], a[0:15]
	ds_read_b128 v[34:37], v80 offset:128
	ds_read_b128 v[54:57], v80 offset:160
	s_waitcnt lgkmcnt(1)
	v_mfma_f32_32x32x16_f16 a[16:31], v[30:33], v[34:37], a[16:31]
	ds_read_b128 v[34:37], v80 offset:17024
	ds_read_b128 v[58:61], v80 offset:17056
	s_waitcnt lgkmcnt(1)
	v_mfma_f32_32x32x16_f16 a[0:15], v[30:33], v[34:37], a[0:15]
	ds_read_b128 v[30:33], v80 offset:192
	ds_read_b128 v[34:37], v80 offset:224
	v_mfma_f32_32x32x16_f16 a[16:31], v[50:53], v[54:57], a[16:31]
	s_waitcnt lgkmcnt(2)
	v_mfma_f32_32x32x16_f16 a[0:15], v[50:53], v[58:61], a[0:15]
	s_waitcnt lgkmcnt(1)
	v_mfma_f32_32x32x16_f16 a[16:31], v[26:29], v[30:33], a[16:31]
	ds_read_b128 v[30:33], v80 offset:17088
	ds_read_b128 v[50:53], v80 offset:17120
	s_waitcnt lgkmcnt(1)
	v_mfma_f32_32x32x16_f16 a[0:15], v[26:29], v[30:33], a[0:15]
	ds_read_b128 v[26:29], v80 offset:256
	ds_read_b128 v[30:33], v80 offset:288
	v_mfma_f32_32x32x16_f16 a[16:31], v[46:49], v[34:37], a[16:31]
	s_waitcnt lgkmcnt(2)
	v_mfma_f32_32x32x16_f16 a[0:15], v[46:49], v[50:53], a[0:15]
	s_waitcnt lgkmcnt(1)
	v_mfma_f32_32x32x16_f16 a[16:31], v[22:25], v[26:29], a[16:31]
	ds_read_b128 v[26:29], v80 offset:17152
	ds_read_b128 v[34:37], v80 offset:17184
	s_waitcnt lgkmcnt(1)
	v_mfma_f32_32x32x16_f16 a[0:15], v[22:25], v[26:29], a[0:15]
	ds_read_b128 v[22:25], v80 offset:320
	ds_read_b128 v[26:29], v80 offset:352
	v_mfma_f32_32x32x16_f16 a[16:31], v[42:45], v[30:33], a[16:31]
	s_waitcnt lgkmcnt(2)
	v_mfma_f32_32x32x16_f16 a[0:15], v[42:45], v[34:37], a[0:15]
	s_waitcnt lgkmcnt(1)
	v_mfma_f32_32x32x16_f16 a[16:31], v[18:21], v[22:25], a[16:31]
	ds_read_b128 v[22:25], v80 offset:17216
	ds_read_b128 v[30:33], v80 offset:17248
	s_waitcnt lgkmcnt(1)
	v_mfma_f32_32x32x16_f16 a[0:15], v[18:21], v[22:25], a[0:15]
	ds_read_b128 v[18:21], v80 offset:384
	ds_read_b128 v[22:25], v80 offset:416
	v_mfma_f32_32x32x16_f16 a[16:31], v[38:41], v[26:29], a[16:31]
	s_waitcnt lgkmcnt(2)
	v_mfma_f32_32x32x16_f16 a[0:15], v[38:41], v[30:33], a[0:15]
	v_and_or_b32 v38, v0, s6, v79
	s_movk_i32 s6, 0x110
	v_mad_u32_u24 v39, v78, s6, v38
	s_waitcnt lgkmcnt(1)
	v_mfma_f32_32x32x16_f16 a[16:31], v[14:17], v[18:21], a[16:31]
	ds_read_b128 v[18:21], v80 offset:17280
	ds_read_b128 v[26:29], v80 offset:17312
	s_waitcnt lgkmcnt(1)
	v_mfma_f32_32x32x16_f16 a[0:15], v[14:17], v[18:21], a[0:15]
	ds_read_b128 v[14:17], v80 offset:448
	ds_read_b128 v[18:21], v80 offset:480
	v_mfma_f32_32x32x16_f16 a[16:31], v[10:13], v[22:25], a[16:31]
	s_waitcnt lgkmcnt(2)
	v_mfma_f32_32x32x16_f16 a[0:15], v[10:13], v[26:29], a[0:15]
	ds_read_b128 v[10:13], v80 offset:17376
	s_waitcnt lgkmcnt(2)
	v_mfma_f32_32x32x16_f16 a[16:31], v[2:5], v[14:17], a[16:31]
	ds_read_b128 v[14:17], v80 offset:17344
	s_waitcnt lgkmcnt(0)
	s_barrier
	v_mfma_f32_32x32x16_f16 a[0:15], v[2:5], v[14:17], a[0:15]
	v_mfma_f32_32x32x16_f16 a[16:31], v[6:9], v[18:21], a[16:31]
	v_mfma_f32_32x32x16_f16 a[0:15], v[6:9], v[10:13], a[0:15]
	s_nop 10
	v_accvgpr_read_b32 v18, a16
	v_accvgpr_read_b32 v19, a17
	v_accvgpr_read_b32 v20, a18
	v_accvgpr_read_b32 v21, a19
	v_accvgpr_read_b32 v22, a20
	v_accvgpr_read_b32 v23, a21
	v_accvgpr_read_b32 v24, a22
	v_accvgpr_read_b32 v25, a23
	v_accvgpr_read_b32 v26, a24
	v_accvgpr_read_b32 v14, a25
	v_accvgpr_read_b32 v15, a26
	v_accvgpr_read_b32 v16, a27
	v_accvgpr_read_b32 v17, a28
	v_accvgpr_read_b32 v27, a29
	v_accvgpr_read_b32 v28, a30
	v_accvgpr_read_b32 v29, a31
	v_cvt_pk_f16_f32 v3, v20, v21
	v_cvt_pk_f16_f32 v2, v18, v19
	v_cvt_pk_f16_f32 v5, v24, v25
	v_cvt_pk_f16_f32 v4, v22, v23
	ds_write2_b64 v39, v[2:3], v[4:5] offset1:2
	v_cvt_pk_f16_f32 v3, v15, v16
	v_cvt_pk_f16_f32 v2, v26, v14
	v_cvt_pk_f16_f32 v5, v28, v29
	v_cvt_pk_f16_f32 v4, v17, v27
	v_accvgpr_read_b32 v6, a0
	v_accvgpr_read_b32 v7, a1
	v_accvgpr_read_b32 v8, a2
	v_accvgpr_read_b32 v9, a3
	v_accvgpr_read_b32 v10, a4
	v_accvgpr_read_b32 v11, a5
	v_accvgpr_read_b32 v12, a6
	v_accvgpr_read_b32 v13, a7
	ds_write2_b64 v39, v[2:3], v[4:5] offset0:4 offset1:6
	v_or_b32_e32 v2, 32, v88
	v_accvgpr_read_b32 v30, a8
	v_accvgpr_read_b32 v31, a9
	v_accvgpr_read_b32 v32, a10
	v_accvgpr_read_b32 v33, a11
	v_accvgpr_read_b32 v34, a12
	v_accvgpr_read_b32 v35, a13
	v_accvgpr_read_b32 v36, a14
	v_accvgpr_read_b32 v37, a15
	v_mad_u32_u24 v14, v2, s6, v38
	v_cvt_pk_f16_f32 v3, v8, v9
	v_cvt_pk_f16_f32 v2, v6, v7
	v_cvt_pk_f16_f32 v5, v12, v13
	v_cvt_pk_f16_f32 v4, v10, v11
	ds_write2_b64 v14, v[2:3], v[4:5] offset1:2
	v_cvt_pk_f16_f32 v3, v32, v33
	v_cvt_pk_f16_f32 v2, v30, v31
	v_cvt_pk_f16_f32 v5, v36, v37
	v_cvt_pk_f16_f32 v4, v34, v35
	v_lshrrev_b32_e32 v8, 4, v0
	ds_write2_b64 v14, v[2:3], v[4:5] offset0:4 offset1:6
	v_and_b32_e32 v4, 0xf0, v82
	v_mov_b32_e32 v5, 0
	v_or_b32_e32 v6, s3, v8
	v_lshl_add_u64 v[2:3], s[4:5], 0, v[4:5]
	v_cmp_gt_i32_e32 vcc, s7, v6
	s_waitcnt lgkmcnt(0)
	s_barrier
	s_and_saveexec_b64 s[4:5], vcc
	s_cbranch_execz .LBB1_35
	v_ashrrev_i32_e32 v7, 31, v6
	v_mad_u32_u24 v5, v8, s6, v4
	v_lshlrev_b64 v[6:7], 8, v[6:7]
	ds_read_b128 v[10:13], v5
	v_lshl_add_u64 v[6:7], v[2:3], 0, v[6:7]
	s_waitcnt lgkmcnt(0)
	global_store_dwordx4 v[6:7], v[10:13], off sc1
	s_nop 1
